# nt hint on the mLSTM chain q/k/v chunk prefetch loads (proj rows are read once)
# speedup vs baseline: 1.0233x; 1.0038x over previous
; #define GAS __attribute__((address_space(1)))
; #define LAS __attribute__((address_space(3)))
; __device__ __forceinline__ void p2_mlstm_chain(Frame& F, const Args& A, int ch) {
;     ...
;       for (int i = tid; i < 64 * 256 / 4; i += NTHREADS) ((LAS unsigned*)(L + ML_CT))[i] = 0u;
;       if (tid < 64) ns[tid] = 0.f;
;       __syncthreads(); }
;     f32x4 Cst[4]; f32x4 Nst = (f32x4){0.f, 0.f, 0.f, 0.f};
; #pragma unroll
;     for (int i = 0; i < 4; ++i) Cst[i] = (f32x4){0.f, 0.f, 0.f, 0.f};
;     u32x4 qreg[2], kreg[2], vreg[4];
;     { const size_t tg0 = (size_t)b * SEQ;
; #pragma unroll
;       for (int j = 0; j < 2; ++j) { const int idx = tid + 512 * j, row = idx >> 3, part = idx & 7; const bf16* src = proj + (tg0 + row) * NP + h * 64 + part * 8; qreg[j] = *(const GAS u32x4*)src; kreg[j] = *(const GAS u32x4*)(src + 256); }
; #pragma unroll
;       for (int j = 0; j < 4; ++j) { const int idx = tid + 512 * j, row = idx >> 4, part = idx & 15; vreg[j] = *(const GAS u32x4*)(proj + (tg0 + row) * NP + 512 + h * 128 + part * 8); } }
.LBB0_374:
	v_writelane_b32 v254, s72, 8
	s_nop 1
	v_writelane_b32 v254, s73, 9
	s_or_b64 exec, exec, s[4:5]
	v_cmp_gt_i32_e64 s[2:3], 64, v48
	s_and_saveexec_b64 s[4:5], s[2:3]
	v_add_u32_e32 v2, 0x14800, v2
	v_mov_b32_e32 v3, 0
	ds_write_b32 v2, v3
	s_or_b64 exec, exec, s[4:5]
	s_lshl_b32 s60, s45, 7
	s_lshl_b32 s2, s45, 9
	s_add_u32 s4, s26, s2
	s_addc_u32 s5, s27, 0
	s_lshl_b64 s[2:3], s[42:43], 11
	s_add_u32 s6, s12, s60
	s_addc_u32 s7, s13, 0
	s_cmp_lt_u32 s68, 64
	s_cselect_b64 s[24:25], -1, 0
	s_cmp_gt_u32 s68, 63
	s_cselect_b64 s[26:27], -1, 0
	s_cmpk_gt_u32 s68, 0xbf
	s_cselect_b64 s[28:29], -1, 0
	s_cmpk_gt_u32 s68, 0x13f
	s_cselect_b64 s[30:31], -1, 0
	s_cmpk_gt_u32 s68, 0x1bf
	v_ashrrev_i32_e32 v38, 4, v48
	s_cselect_b64 s[82:83], -1, 0
	s_cmp_eq_u32 s98, 1
	v_lshlrev_b32_e32 v50, 4, v48
	v_ashrrev_i32_e32 v39, 31, v38
	s_cselect_b64 s[34:35], -1, 0
	s_cmp_eq_u32 s98, 2
	v_and_b32_e32 v106, 0x70, v50
	v_mov_b32_e32 v107, 0
	s_movk_i32 s46, 0x1400
	v_lshl_add_u64 v[20:21], s[2:3], 0, v[38:39]
	v_mov_b64_e32 v[28:29], s[12:13]
	v_ashrrev_i32_e32 v40, 4, v18
	v_ashrrev_i32_e32 v42, 4, v1
	v_ashrrev_i32_e32 v44, 4, v26
	v_lshrrev_b32_e32 v52, 4, v49
	s_cselect_b64 s[36:37], -1, 0
	s_cmp_eq_u32 s98, 3
	v_lshl_add_u64 v[10:11], s[6:7], 0, v[106:107]
	v_ashrrev_i32_e32 v34, 3, v48
	v_ashrrev_i32_e32 v36, 3, v18
	v_mad_u64_u32 v[22:23], s[6:7], v20, s46, v[28:29]
	v_ashrrev_i32_e32 v41, 31, v40
	v_ashrrev_i32_e32 v43, 31, v42
	v_ashrrev_i32_e32 v45, 31, v44
	s_mov_b32 s23, 0
	s_cselect_b64 s[38:39], -1, 0
	v_lshlrev_b32_e32 v53, 3, v48
	v_ashrrev_i32_e32 v35, 31, v34
	v_ashrrev_i32_e32 v37, 31, v36
	v_mad_i32_i24 v23, v21, s46, v23
	s_lshl_b32 s22, s45, 8
	v_lshl_add_u64 v[18:19], s[2:3], 0, v[40:41]
	v_lshl_add_u64 v[30:31], s[2:3], 0, v[42:43]
	v_lshl_add_u64 v[26:27], s[2:3], 0, v[44:45]
	v_lshlrev_b32_e32 v68, 2, v52
	v_lshlrev_b32_e32 v146, 5, v52
	v_lshlrev_b32_e32 v39, 3, v52
	v_lshlrev_b32_e32 v52, 1, v52
	v_lshl_add_u64 v[2:3], s[2:3], 0, v[34:35]
	v_lshl_add_u64 v[12:13], s[2:3], 0, v[36:37]
	v_lshl_add_u64 v[20:21], v[22:23], 0, s[22:23]
	v_mad_u64_u32 v[22:23], s[6:7], v18, s46, v[28:29]
	v_mad_u64_u32 v[32:33], s[6:7], v30, s46, v[28:29]
	v_mad_u64_u32 v[28:29], s[2:3], v26, s46, v[28:29]
	v_lshrrev_b32_e32 v37, 1, v48
	v_bfe_u32 v70, v48, 2, 2
	v_and_b32_e32 v43, 24, v53
	v_xor_b32_e32 v53, v52, v68
	v_mad_i32_i24 v23, v19, s46, v23
	v_mad_i32_i24 v33, v31, s46, v33
	v_mad_i32_i24 v29, v27, s46, v29
	v_and_or_b32 v74, v53, 4, v70
	v_and_b32_e32 v77, 2, v52
	v_and_b32_e32 v52, 3, v48
	v_bitop3_b32 v37, v37, 4, v48 bitop3:0x48
	v_lshrrev_b32_e32 v53, 2, v34
	v_and_b32_e32 v64, 15, v48
	v_and_b32_e32 v106, 0xf0, v50
	v_lshl_add_u64 v[18:19], v[22:23], 0, s[22:23]
	v_lshl_add_u64 v[30:31], v[32:33], 0, s[22:23]
	v_lshl_add_u64 v[26:27], v[28:29], 0, s[22:23]
	v_bfe_u32 v35, v48, 1, 2
	v_bitop3_b32 v37, v37, s98, v52 bitop3:0x36
	v_bfe_u32 v52, v34, 1, 1
	v_and_b32_e32 v53, 2, v53
	v_lshrrev_b32_e32 v59, 2, v36
	v_lshl_add_u64 v[20:21], v[20:21], 0, v[106:107]
	v_lshl_add_u64 v[22:23], v[18:19], 0, v[106:107]
	v_lshl_add_u64 v[30:31], v[30:31], 0, v[106:107]
	v_lshl_add_u64 v[32:33], v[26:27], 0, v[106:107]
	v_lshrrev_b32_e32 v58, 5, v49
	s_add_i32 s8, 0, 0x10800
	v_and_b32_e32 v106, 48, v49
	v_lshlrev_b32_e32 v49, 8, v64
	v_lshlrev_b32_e32 v37, 5, v37
	v_bitop3_b32 v52, v52, v35, v53 bitop3:0x36
	v_bfe_u32 v57, v36, 1, 1
	v_and_b32_e32 v59, 2, v59
	v_add3_u32 v49, s8, v49, v37
	v_lshlrev_b32_e32 v37, 7, v34
	v_lshlrev_b32_e32 v52, 5, v52
	v_bitop3_b32 v35, v57, v35, v59 bitop3:0x36
	v_add3_u32 v52, 0, v37, v52
	v_lshlrev_b32_e32 v37, 7, v36
	v_lshlrev_b32_e32 v35, 5, v35
	v_lshrrev_b32_e32 v59, 1, v38
	v_bfe_u32 v55, v48, 1, 3
	v_add3_u32 v57, 0, v37, v35
	v_and_b32_e32 v37, 3, v38
	v_bitop3_b32 v59, v59, 4, v38 bitop3:0x48
	v_mad_u64_u32 v[6:7], s[6:7], v2, s46, v[10:11]
	v_mad_u64_u32 v[14:15], s[6:7], v12, s46, v[10:11]
	v_bitop3_b32 v37, v59, v55, v37 bitop3:0x36
	v_mad_i32_i24 v7, v3, s46, v7
	v_mad_i32_i24 v15, v13, s46, v15
	v_lshlrev_b32_e32 v35, 8, v38
	v_lshlrev_b32_e32 v37, 5, v37
	v_lshrrev_b32_e32 v60, 1, v40
	s_waitcnt lgkmcnt(0)
	s_barrier
	global_load_dwordx4 v[2:5], v[6:7], off nt
	s_nop 0
	global_load_dwordx4 v[6:9], v[6:7], off offset:512 nt
	s_nop 0
	global_load_dwordx4 v[10:13], v[14:15], off nt
	s_nop 0
	global_load_dwordx4 v[14:17], v[14:15], off offset:512 nt
	s_nop 0
	global_load_dwordx4 v[18:21], v[20:21], off offset:1024 nt
	s_nop 0
	global_load_dwordx4 v[22:25], v[22:23], off offset:1024 nt
	s_nop 0
	global_load_dwordx4 v[26:29], v[30:31], off offset:1024 nt
	s_nop 0
	global_load_dwordx4 v[30:33], v[32:33], off offset:1024 nt
	v_add3_u32 v59, 0, v35, v37
	v_and_b32_e32 v37, 3, v40
	v_bitop3_b32 v60, v60, 4, v40 bitop3:0x48
	v_bitop3_b32 v37, v60, v55, v37 bitop3:0x36
	v_lshlrev_b32_e32 v35, 8, v40
	v_lshlrev_b32_e32 v37, 5, v37
	v_lshrrev_b32_e32 v61, 1, v42
	v_add3_u32 v60, 0, v35, v37
	v_and_b32_e32 v37, 3, v42
	v_bitop3_b32 v61, v61, 4, v42 bitop3:0x48
	v_bitop3_b32 v37, v61, v55, v37 bitop3:0x36
	v_lshlrev_b32_e32 v35, 8, v42
	v_lshlrev_b32_e32 v37, 5, v37
	v_lshrrev_b32_e32 v62, 1, v44
	v_or_b32_e32 v54, s44, v64
	v_and_b32_e32 v1, 7, v48
	s_movk_i32 s6, 0x90
	v_add3_u32 v61, 0, v35, v37
	v_and_b32_e32 v37, 3, v44
	v_bitop3_b32 v62, v62, 4, v44 bitop3:0x48
	v_lshlrev_b32_e32 v63, 4, v1
	v_mul_lo_u32 v1, v54, s6
	v_bitop3_b32 v37, v62, v55, v37 bitop3:0x36
	v_and_b32_e32 v41, 16, v50
	v_add_u32_e32 v50, 0, v1
	v_lshrrev_b32_e32 v1, 2, v48
	v_lshlrev_b32_e32 v35, 8, v44
	v_lshlrev_b32_e32 v37, 5, v37
	v_bfe_u32 v56, v48, 1, 1
	v_and_b32_e32 v66, 2, v1
	v_and_b32_e32 v69, 16, v48
; __device__ __forceinline__ void p2_mlstm_chain(Frame& F, const Args& A, int ch) {
;     ...
;         const size_t tg0 = (size_t)b * SEQ + c * 128; const int t = 16 * w + tl;
; #pragma unroll
;         for (int j = 0; j < 2; ++j) { const int idx = tid + 512 * j, row = idx >> 3, part = idx & 7; *(LAS u32x4*)(L + ML_QS + row * 144 + part * 16) = qreg[j];
;             *(LAS u32x4*)(L + ML_KS + 128 * row + 32 * ((part >> 1) ^ swzg(row)) + 16 * (part & 1)) = kreg[j]; }
; #pragma unroll
;         for (int j = 0; j < 4; ++j) { const int idx = tid + 512 * j, row = idx >> 4, part = idx & 15; *(LAS u32x4*)(L + ML_VS + 256 * row + 32 * ((part >> 1) ^ swzf(row)) + 16 * (part & 1)) = vreg[j]; }
;         const float mc = sMC[c], Mn = sMC[32 + c], Mt = sM[c * 128 + t], lf = sLF[c * 128 + t];
;         if (tid < 128) sWK[tid] = __builtin_amdgcn_exp2f((sA[c * 128 + tid] - Mn) * 1.4426950408889634f);
;         __syncthreads();
;         if (c < 15) { const size_t tn = tg0 + 128;
; #pragma unroll
;             for (int j = 0; j < 2; ++j) { const int idx = tid + 512 * j, row = idx >> 3, part = idx & 7; const bf16* src = proj + (tn + row) * NP + h * 64 + part * 8; qreg[j] = *(const GAS u32x4*)src; kreg[j] = *(const GAS u32x4*)(src + 256); }
; #pragma unroll
;             for (int j = 0; j < 4; ++j) { const int idx = tid + 512 * j, row = idx >> 4, part = idx & 15; vreg[j] = *(const GAS u32x4*)(proj + (tn + row) * NP + 512 + h * 128 + part * 8); } }
;         u32x2 og[8];
; #pragma unroll
;         for (int vb = 0; vb < 8; ++vb) og[vb] = *(const GAS u32x2*)(proj + (tg0 + t) * NP + 1024 + h * 128 + 16 * vb + 4 * fq);
;         bf16x8 qf[2];
; #pragma unroll
;         for (int ds = 0; ds < 2; ++ds) qf[ds] = *(const LAS bf16x8*)(L + ML_QS + t * 144 + ds * 64 + fq * 16);
;         unsigned sfr[4][4];
; #pragma unroll
;         for (int i = 0; i < 4; ++i)
; #pragma unroll
;             for (int j = 0; j < 4; ++j) sfr[i][j] = 0u;
;         float den = 0.f;
; #pragma unroll
;         for (int sb = 0; sb < 8; ++sb) {
;             if (sb <= w) {
;                 f32x4 G = (f32x4){0.f, 0.f, 0.f, 0.f}; const int sr = 16 * sb + tl;
; #pragma unroll
;                 for (int ds = 0; ds < 2; ++ds) { const bf16x8 a = *(const LAS bf16x8*)(L + ML_KS + 128 * sr + 32 * ((2 * ds + (fq >> 1)) ^ swzg(sr)) + 16 * (fq & 1)); G = __builtin_amdgcn_mfma_f32_16x16x32_bf16(a, qf[ds], G, 0, 0, 0); }
	v_add3_u32 v62, 0, v35, v37
	v_lshlrev_b32_e32 v35, 7, v64
	v_or_b32_e32 v67, v56, v66
	v_add3_u32 v55, 0, v69, v35
	v_bitop3_b32 v35, v56, v58, v66 bitop3:0x36
	v_lshlrev_b32_e32 v56, 5, v35
	v_bitop3_b32 v35, v58, v67, 2 bitop3:0x36
	v_lshlrev_b32_e32 v58, 5, v35
	v_or_b32_e32 v35, 3, v68
	v_cmp_gt_u32_e64 s[10:11], v35, v54
	v_or_b32_e32 v35, 17, v68
	v_or_b32_e32 v37, 2, v68
	v_cmp_gt_u32_e64 s[48:49], v35, v54
	v_cmp_gt_u32_e64 s[12:13], v37, v54
	v_or_b32_e32 v37, 16, v68
	v_writelane_b32 v254, s48, 10
	v_or_b32_e32 v35, 19, v68
	v_xor_b32_e32 v66, 16, v46
	v_writelane_b32 v254, s49, 11
	v_cmp_gt_u32_e64 s[48:49], v37, v54
	v_or_b32_e32 v37, 18, v68
	v_add_u32_e32 v47, 64, v47
	v_writelane_b32 v254, s48, 12
	s_and_b64 s[40:41], s[40:41], vcc
	v_cmp_lt_i32_e32 vcc, v66, v47
	v_writelane_b32 v254, s49, 13
	v_cmp_gt_u32_e64 s[48:49], v35, v54
	v_or_b32_e32 v35, 33, v68
	v_cndmask_b32_e32 v69, v46, v66, vcc
	v_writelane_b32 v254, s48, 14
	v_xor_b32_e32 v66, 32, v46
	v_cmp_lt_i32_e32 vcc, v66, v47
	v_writelane_b32 v254, s49, 15
	v_cmp_gt_u32_e64 s[48:49], v37, v54
	v_or_b32_e32 v37, 32, v68
	v_cndmask_b32_e32 v79, v46, v66, vcc
	v_writelane_b32 v254, s48, 16
	v_add_u32_e32 v46, s44, v64
	v_mov_b32_e32 v47, v107
	v_writelane_b32 v254, s49, 17
	v_cmp_gt_u32_e64 s[48:49], v35, v54
	v_or_b32_e32 v35, 35, v68
	v_and_b32_e32 v51, 48, v48
	v_writelane_b32 v254, s48, 18
	v_lshlrev_b64 v[66:67], 11, v[46:47]
	v_lshrrev_b32_e32 v81, 1, v51
	v_writelane_b32 v254, s49, 19
	v_cmp_gt_u32_e64 s[48:49], v37, v54
	v_or_b32_e32 v37, 34, v68
	s_mov_b64 s[44:45], 0x5000080
	v_writelane_b32 v254, s48, 20
	v_mov_b32_e32 v80, 0xa00000
	v_or_b32_e32 v76, 4, v70
	v_writelane_b32 v254, s49, 21
	v_cmp_gt_u32_e64 s[48:49], v35, v54
	v_or_b32_e32 v35, 49, v68
	v_or_b32_e32 v87, v39, v76
	v_writelane_b32 v254, s48, 22
	v_lshrrev_b32_e32 v89, 1, v87
	v_and_b32_e32 v90, 4, v89
	v_writelane_b32 v254, s49, 23
	v_cmp_gt_u32_e64 s[48:49], v37, v54
	v_or_b32_e32 v37, 48, v68
	v_bitop3_b32 v90, v90, s98, v70 bitop3:0x36
	v_writelane_b32 v254, s48, 24
	v_lshlrev_b32_e32 v90, 5, v90
	v_lshlrev_b32_e32 v88, 8, v87
	v_writelane_b32 v254, s49, 25
	v_cmp_gt_u32_e64 s[48:49], v35, v54
	v_or_b32_e32 v35, 51, v68
	v_xor_b32_e32 v90, 0x80, v90
	v_writelane_b32 v254, s48, 26
	v_add3_u32 v88, 0, v90, v88
	v_and_b32_e32 v71, 4, v68
	v_writelane_b32 v254, s49, 27
	v_cmp_gt_u32_e64 s[48:49], v37, v54
	v_or_b32_e32 v37, 50, v68
	v_or_b32_e32 v72, v71, v70
	v_writelane_b32 v254, s48, 28
	s_movk_i32 s22, 0x80
	v_add_u32_e32 v73, s8, v43
	v_writelane_b32 v254, s49, 29
	v_cmp_gt_u32_e64 s[48:49], v35, v54
	v_or_b32_e32 v35, 0x41, v68
	v_cmp_gt_i32_e64 s[2:3], s22, v48
	v_writelane_b32 v254, s48, 30
	v_lshlrev_b32_e32 v65, 2, v48
	v_lshrrev_b32_e32 v78, 3, v48
	v_writelane_b32 v254, s49, 31
	v_cmp_gt_u32_e64 s[48:49], v37, v54
	v_or_b32_e32 v37, 64, v68
	v_mul_lo_u32 v48, v34, s6
	v_writelane_b32 v254, s48, 32
	v_mul_lo_u32 v53, v36, s6
	v_bitop3_b32 v71, v71, s98, v70 bitop3:0x36
	v_writelane_b32 v254, s49, 33
	v_cmp_gt_u32_e64 s[48:49], v35, v54
	v_or_b32_e32 v35, 0x43, v68
	v_add_u32_e32 v75, 0, v43
	v_writelane_b32 v254, s48, 34
	v_lshl_add_u32 v71, v71, 5, 0
	s_add_i32 s7, 0, 0x14a00
	v_writelane_b32 v254, s49, 35
	v_cmp_gt_u32_e64 s[48:49], v37, v54
	v_or_b32_e32 v37, 0x42, v68
	v_and_or_b32 v78, v78, 1, v77
	v_writelane_b32 v254, s48, 36
	v_add_u32_e32 v1, s7, v65
	v_add_u32_e32 v147, s7, v146
	v_writelane_b32 v254, s49, 37
	s_lshl_b64 s[48:49], s[42:43], 22
	s_lshl_b32 s43, s33, 8
	v_lshl_add_u64 v[66:67], s[48:49], 0, v[66:67]
	s_and_b32 s50, s43, 0x300
	v_or3_b32 v66, v66, s50, v81
	v_lshl_add_u64 v[66:67], s[58:59], 0, v[66:67]
	v_lshl_add_u64 v[110:111], v[66:67], 0, s[44:45]
	v_mad_i64_i32 v[66:67], s[44:45], v38, s46, 0
	v_mad_i64_i32 v[66:67], s[44:45], s42, v80, v[66:67]
	v_lshlrev_b32_e32 v38, 4, v64
	v_or3_b32 v66, v66, s50, v38
	v_lshl_add_u64 v[66:67], s[58:59], 0, v[66:67]
	s_mov_b64 s[44:45], 0x270a0400
	v_lshl_add_u64 v[112:113], v[66:67], 0, s[44:45]
	v_mad_i64_i32 v[66:67], s[48:49], v40, s46, 0
	v_mad_i64_i32 v[66:67], s[48:49], s42, v80, v[66:67]
	v_or3_b32 v66, v66, s50, v38
	v_lshl_add_u64 v[66:67], s[58:59], 0, v[66:67]
	v_lshl_add_u64 v[114:115], v[66:67], 0, s[44:45]
	v_mad_i64_i32 v[66:67], s[48:49], v42, s46, 0
	v_mad_i64_i32 v[66:67], s[48:49], s42, v80, v[66:67]
	v_or3_b32 v66, v66, s50, v38
	v_lshl_add_u64 v[66:67], s[58:59], 0, v[66:67]
	v_or_b32_e32 v42, 32, v39
	v_lshl_add_u64 v[116:117], v[66:67], 0, s[44:45]
	v_mad_i64_i32 v[66:67], s[48:49], v44, s46, 0
	v_or_b32_e32 v44, v42, v70
	v_or_b32_e32 v42, v42, v76
	v_lshrrev_b32_e32 v91, 1, v42
	v_and_b32_e32 v92, 4, v91
	v_bitop3_b32 v92, v92, s98, v70 bitop3:0x36
	v_lshlrev_b32_e32 v92, 5, v92
	v_lshlrev_b32_e32 v90, 8, v42
	v_xor_b32_e32 v92, 0x80, v92
	v_add3_u32 v90, 0, v92, v90
	v_or_b32_e32 v92, 64, v39
	v_or_b32_e32 v93, v92, v70
	v_or_b32_e32 v92, v92, v76
	v_lshrrev_b32_e32 v96, 1, v92
	v_and_b32_e32 v97, 4, v96
	v_mad_i64_i32 v[66:67], s[48:49], s42, v80, v[66:67]
	v_bitop3_b32 v97, v97, s98, v70 bitop3:0x36
	v_or3_b32 v66, v66, s50, v38
	v_or_b32_e32 v38, 0x51, v68
	v_lshlrev_b32_e32 v97, 5, v97
	v_lshl_add_u64 v[66:67], s[58:59], 0, v[66:67]
	v_cmp_gt_u32_e64 s[48:49], v38, v54
	v_lshlrev_b32_e32 v38, 5, v72
	v_lshlrev_b32_e32 v95, 8, v92
	v_xor_b32_e32 v97, 0x80, v97
	v_lshl_add_u64 v[118:119], v[66:67], 0, s[44:45]
	v_cmp_gt_u32_e64 s[44:45], v35, v54
	v_xad_u32 v149, v38, s22, v73
	s_movk_i32 s22, 0xa0
	v_add3_u32 v95, 0, v97, v95
	v_or_b32_e32 v97, 0x60, v39
	v_writelane_b32 v254, s44, 38
	v_xad_u32 v150, v38, s22, v73
	s_movk_i32 s22, 0xc0
	v_or_b32_e32 v76, v97, v76
	v_writelane_b32 v254, s45, 39
; #define GAS __attribute__((address_space(1)))
; #define LAS __attribute__((address_space(3)))
; __device__ __forceinline__ int swzf(int r) { return (r & 3) | ((((r >> 2) ^ (r >> 3)) & 1) << 2); }
; __device__ __forceinline__ int swzg(int r) { return ((r >> 1) & 1) | (((r >> 3) & 1) << 1); }
; __device__ __forceinline__ void p2_mlstm_chain(Frame& F, const Args& A, int ch) {
;     ...
;         const size_t tg0 = (size_t)b * SEQ + c * 128; const int t = 16 * w + tl;
; #pragma unroll
;         for (int j = 0; j < 2; ++j) { const int idx = tid + 512 * j, row = idx >> 3, part = idx & 7; *(LAS u32x4*)(L + ML_QS + row * 144 + part * 16) = qreg[j];
;             *(LAS u32x4*)(L + ML_KS + 128 * row + 32 * ((part >> 1) ^ swzg(row)) + 16 * (part & 1)) = kreg[j]; }
; #pragma unroll
;         for (int j = 0; j < 4; ++j) { const int idx = tid + 512 * j, row = idx >> 4, part = idx & 15; *(LAS u32x4*)(L + ML_VS + 256 * row + 32 * ((part >> 1) ^ swzf(row)) + 16 * (part & 1)) = vreg[j]; }
;         const float mc = sMC[c], Mn = sMC[32 + c], Mt = sM[c * 128 + t], lf = sLF[c * 128 + t];
;         if (tid < 128) sWK[tid] = __builtin_amdgcn_exp2f((sA[c * 128 + tid] - Mn) * 1.4426950408889634f);
;         __syncthreads();
;         if (c < 15) { const size_t tn = tg0 + 128;
; #pragma unroll
;             for (int j = 0; j < 2; ++j) { const int idx = tid + 512 * j, row = idx >> 3, part = idx & 7; const bf16* src = proj + (tn + row) * NP + h * 64 + part * 8; qreg[j] = *(const GAS u32x4*)src; kreg[j] = *(const GAS u32x4*)(src + 256); }
; #pragma unroll
;             for (int j = 0; j < 4; ++j) { const int idx = tid + 512 * j, row = idx >> 4, part = idx & 15; vreg[j] = *(const GAS u32x4*)(proj + (tn + row) * NP + 512 + h * 128 + part * 8); } }
;         u32x2 og[8];
; #pragma unroll
;         for (int vb = 0; vb < 8; ++vb) og[vb] = *(const GAS u32x2*)(proj + (tg0 + t) * NP + 1024 + h * 128 + 16 * vb + 4 * fq);
;         bf16x8 qf[2];
; #pragma unroll
;         for (int ds = 0; ds < 2; ++ds) qf[ds] = *(const LAS bf16x8*)(L + ML_QS + t * 144 + ds * 64 + fq * 16);
	v_mad_i64_i32 v[34:35], s[44:45], v34, s46, 0
	v_mad_i64_i32 v[66:67], s[44:45], v36, s46, 0
	v_mad_u64_u32 v[46:47], s[44:45], v46, s46, 0
	v_xad_u32 v151, v38, s22, v73
	s_movk_i32 s22, 0x60
	v_lshrrev_b32_e32 v99, 1, v76
	v_cmp_gt_u32_e64 s[46:47], v37, v54
	v_or_b32_e32 v40, 0x50, v68
	v_mad_i64_i32 v[36:37], s[44:45], s42, v80, v[34:35]
	v_mad_i64_i32 v[34:35], s[44:45], s42, v80, v[66:67]
	v_mad_i64_i32 v[46:47], s[42:43], s42, v80, v[46:47]
	v_xad_u32 v152, v38, s22, v73
	s_movk_i32 s22, 0xe0
	v_and_b32_e32 v100, 4, v99
	v_xad_u32 v153, v38, s22, v73
	v_or3_b32 v46, v46, s50, v81
	v_cmp_gt_u32_e64 s[50:51], v40, v54
	v_or_b32_e32 v40, v39, v70
	v_add_u32_e32 v157, v73, v38
	v_xad_u32 v159, v38, 32, v73
	v_xad_u32 v160, v38, 64, v73
	v_or_b32_e32 v38, v68, v70
	v_or_b32_e32 v98, v97, v70
	v_bitop3_b32 v70, v100, s98, v70 bitop3:0x36
	v_lshlrev_b32_e32 v156, 8, v40
	v_lshlrev_b32_e32 v158, 8, v44
	v_lshl_add_u32 v163, v40, 7, v75
	v_and_or_b32 v40, v89, 1, v77
	v_lshl_add_u32 v170, v44, 7, v75
	v_and_or_b32 v44, v91, 1, v77
	v_lshl_add_u32 v94, v93, 8, v71
	v_lshl_add_u32 v173, v93, 7, v75
	v_and_or_b32 v93, v96, 1, v77
	v_lshlrev_b32_e32 v70, 5, v70
	v_and_or_b32 v77, v99, 1, v77
	s_add_i32 s7, 0, 0x14800
	v_lshl_add_u64 v[46:47], s[58:59], 0, v[46:47]
	s_mov_b64 s[42:43], 0x27000880
	v_lshlrev_b32_e32 v162, 5, v74
	v_lshlrev_b32_e32 v166, 5, v40
	v_lshlrev_b32_e32 v172, 5, v44
	v_lshlrev_b32_e32 v175, 5, v93
	v_lshlrev_b32_e32 v97, 8, v76
	v_xor_b32_e32 v70, 0x80, v70
	v_lshlrev_b32_e32 v178, 5, v77
	v_add_u32_e32 v45, 0, v63
	v_lshrrev_b32_e32 v233, 7, v0
	v_cmp_eq_u32_e64 s[98:99], 0, v233
	s_and_saveexec_b64 s[100:101], s[98:99]
	v_lshlrev_b32_e32 v232, 2, v0
	global_load_dword v233, v232, s[4:5]
	v_add_u32_e32 v232, 0x1c000, v232
	s_waitcnt vmcnt(0)
	ds_write_b32 v232, v233
	s_or_b64 exec, exec, s[100:101]
	s_sub_i32 s98, 11, s93
	s_cmp_lt_u32 s93, 4
	s_cselect_b32 s98, s93, s98
	v_bfe_u32 v252, v0, 4, 2
	v_lshlrev_b32_e32 v252, 4, v252
	v_add_u32_e32 v252, 0x1c000, v252
	v_lshl_add_u64 v[108:109], s[4:5], 0, v[106:107]
	v_cmp_eq_u32_e64 s[4:5], 0, v64
	v_lshl_add_u32 v148, v54, 2, s7
	v_cmp_gt_u32_e64 s[6:7], v68, v54
	v_cmp_lt_u32_e64 s[8:9], v68, v54
	v_lshl_add_u64 v[120:121], v[46:47], 0, s[42:43]
	v_or_b32_e32 v66, 0x53, v68
	v_or_b32_e32 v67, 0x52, v68
	v_or_b32_e32 v72, 0x61, v68
	v_or_b32_e32 v80, 0x60, v68
	v_or_b32_e32 v81, 0x63, v68
	v_or_b32_e32 v82, 0x62, v68
	v_or_b32_e32 v83, 0x71, v68
	v_or_b32_e32 v84, 0x70, v68
	v_or_b32_e32 v85, 0x73, v68
	v_or_b32_e32 v86, 0x72, v68
	v_lshlrev_b32_e32 v154, 2, v69
	v_lshlrev_b32_e32 v155, 2, v79
	v_lshl_add_u32 v161, v38, 8, v75
	v_xor_b32_e32 v38, 32, v162
	v_xor_b32_e32 v46, 64, v162
	v_xor_b32_e32 v47, 0x60, v162
	v_xor_b32_e32 v68, 0x80, v162
	v_xor_b32_e32 v69, 0xa0, v162
	v_xor_b32_e32 v73, 0xc0, v162
	v_xor_b32_e32 v74, 0xe0, v162
	v_add_u32_e32 v79, v71, v156
	v_lshl_add_u32 v164, v87, 7, v75
	v_lshlrev_b32_e32 v165, 5, v78
	v_xor_b32_e32 v40, 32, v166
	v_xor_b32_e32 v78, 64, v166
	v_xor_b32_e32 v87, 0x60, v166
	v_add_u32_e32 v89, v71, v158
	v_lshl_add_u32 v171, v42, 7, v75
	v_xor_b32_e32 v42, 32, v172
	v_xor_b32_e32 v44, 64, v172
	v_xor_b32_e32 v91, 0x60, v172
	v_lshl_add_u32 v174, v92, 7, v75
	v_xor_b32_e32 v92, 32, v175
	v_xor_b32_e32 v93, 64, v175
	v_xor_b32_e32 v96, 0x60, v175
	v_lshl_add_u32 v71, v98, 8, v71
	v_add3_u32 v70, 0, v70, v97
	v_lshl_add_u32 v176, v98, 7, v75
	v_lshl_add_u32 v177, v76, 7, v75
	v_xor_b32_e32 v75, 32, v178
	v_xor_b32_e32 v76, 64, v178
	v_xor_b32_e32 v77, 0x60, v178
	v_lshlrev_b32_e32 v64, 2, v64
	v_or3_b32 v36, v36, s60, v63
	v_or3_b32 v34, v34, s60, v63
	v_xor_b32_e32 v167, 32, v165
	v_xor_b32_e32 v168, 64, v165
	v_xor_b32_e32 v169, 0x60, v165
	v_add_u32_e32 v179, 0x15000, v65
	v_lshl_or_b32 v180, s98, 6, v64
	v_lshl_add_u64 v[122:123], s[58:59], 0, v[36:37]
	v_lshl_add_u64 v[124:125], s[58:59], 0, v[34:35]
	v_mov_b32_e32 v34, v107
	v_mov_b32_e32 v35, v107
	v_mov_b32_e32 v36, v107
	v_mov_b32_e32 v37, v107
	v_add_u32_e32 v181, v45, v48
	v_add_u32_e32 v182, v52, v41
	v_add_u32_e32 v183, v45, v53
	v_add_u32_e32 v184, v57, v41
	v_add_u32_e32 v185, v59, v41
	v_add_u32_e32 v186, v60, v41
	v_add_u32_e32 v187, v61, v41
	v_add_u32_e32 v188, v62, v41
	v_add_u32_e32 v189, v50, v51
	v_mov_b32_e32 v190, 0x358637bd
	v_add_u32_e32 v191, v79, v43
	v_add_u32_e32 v192, v88, v43
	v_add_u32_e32 v193, v164, v40
	v_add_u32_e32 v194, v164, v78
	v_add_u32_e32 v195, v164, v87
	v_add_u32_e32 v196, v89, v43
	v_add_u32_e32 v197, v90, v43
	v_add_u32_e32 v198, v171, v42
	v_add_u32_e32 v199, v171, v44
	v_add_u32_e32 v200, v171, v91
	v_add_u32_e32 v201, v94, v43
	v_add_u32_e32 v202, v95, v43
	v_add_u32_e32 v203, v174, v92
	v_add_u32_e32 v204, v174, v93
	v_add_u32_e32 v205, v174, v96
	v_add_u32_e32 v206, v71, v43
	v_add_u32_e32 v207, v70, v43
	v_add_u32_e32 v208, v177, v75
	v_add_u32_e32 v209, v177, v76
	v_add_u32_e32 v210, v177, v77
	v_add_u32_e32 v211, v49, v39
	v_add_u32_e32 v212, v55, v56
	v_add_u32_e32 v213, v55, v58
	v_add_u32_e32 v214, v161, v38
	v_add_u32_e32 v215, v161, v46
	v_add_u32_e32 v216, v161, v47
	v_add_u32_e32 v217, v161, v68
	v_add_u32_e32 v218, v161, v69
	v_add_u32_e32 v219, v161, v73
	v_add_u32_e32 v220, v161, v74
	v_mov_b32_e32 v50, v107
	v_mov_b32_e32 v51, v107
	v_mov_b32_e32 v52, v107
	v_mov_b32_e32 v53, v107
	v_mov_b32_e32 v46, v107
	v_mov_b32_e32 v47, v107
	v_mov_b32_e32 v48, v107
	v_mov_b32_e32 v49, v107
	v_mov_b32_e32 v42, v107
	v_mov_b32_e32 v43, v107
	v_mov_b32_e32 v44, v107
	v_mov_b32_e32 v45, v107
	v_mov_b32_e32 v38, v107
	v_mov_b32_e32 v39, v107
	v_mov_b32_e32 v40, v107
	v_mov_b32_e32 v41, v107
	v_cmp_gt_u32_e64 s[86:87], v66, v54
	v_cmp_gt_u32_e64 s[90:91], v67, v54
	v_cmp_gt_u32_e64 s[44:45], v72, v54
	v_cmp_gt_u32_e64 s[94:95], v80, v54
	v_cmp_gt_u32_e64 s[60:61], v81, v54
	v_cmp_gt_u32_e64 s[62:63], v82, v54
	v_cmp_gt_u32_e64 s[64:65], v83, v54
	v_cmp_gt_u32_e64 s[66:67], v84, v54
	v_cmp_gt_u32_e64 s[68:69], v85, v54
	v_cmp_gt_u32_e64 s[70:71], v86, v54
	s_mov_b64 s[42:43], 0
	s_mov_b32 s22, 0x3e000000
	global_load_dwordx2 v[140:141], v[120:121], off offset:-128
	global_load_dwordx2 v[138:139], v[120:121], off offset:-96
	global_load_dwordx2 v[136:137], v[120:121], off offset:-64
	global_load_dwordx2 v[134:135], v[120:121], off offset:-32
	global_load_dwordx2 v[132:133], v[120:121], off
	global_load_dwordx2 v[130:131], v[120:121], off offset:32
	global_load_dwordx2 v[128:129], v[120:121], off offset:64
	global_load_dwordx2 v[126:127], v[120:121], off offset:96
	s_branch .LBB0_378

; #define GAS __attribute__((address_space(1)))
; __device__ __forceinline__ void p2_mlstm_chain(Frame& F, const Args& A, int ch) {
;     ...
;         __syncthreads();
;         if (c < 15) { const size_t tn = tg0 + 128;
; #pragma unroll
;             for (int j = 0; j < 2; ++j) { const int idx = tid + 512 * j, row = idx >> 3, part = idx & 7; const bf16* src = proj + (tn + row) * NP + h * 64 + part * 8; qreg[j] = *(const GAS u32x4*)src; kreg[j] = *(const GAS u32x4*)(src + 256); }
; #pragma unroll
;             for (int j = 0; j < 4; ++j) { const int idx = tid + 512 * j, row = idx >> 4, part = idx & 15; vreg[j] = *(const GAS u32x4*)(proj + (tn + row) * NP + 512 + h * 128 + part * 8); } }
.LBB0_380:
	s_or_b64 exec, exec, s[72:73]
	s_cmp_eq_u32 s42, 0x960000
	s_waitcnt lgkmcnt(0)
	s_barrier
	s_cbranch_scc1 .LBB0_382
	v_lshl_add_u64 v[2:3], v[122:123], 0, s[42:43]
	v_add_co_u32_e32 v6, vcc, 0x270a0000, v2
	v_lshl_add_u64 v[10:11], v[124:125], 0, s[42:43]
	s_nop 0
	v_addc_co_u32_e32 v7, vcc, 0, v3, vcc
	v_add_co_u32_e32 v14, vcc, 0x270a0000, v10
	v_lshl_add_u64 v[18:19], v[112:113], 0, s[42:43]
	s_nop 0
	v_addc_co_u32_e32 v15, vcc, 0, v11, vcc
	v_lshl_add_u64 v[22:23], v[114:115], 0, s[42:43]
	v_lshl_add_u64 v[26:27], v[116:117], 0, s[42:43]
	v_lshl_add_u64 v[30:31], v[118:119], 0, s[42:43]
	global_load_dwordx4 v[2:5], v[6:7], off nt
	s_nop 0
	global_load_dwordx4 v[6:9], v[6:7], off offset:512 nt
	s_nop 0
	global_load_dwordx4 v[10:13], v[14:15], off nt
	s_nop 0
	global_load_dwordx4 v[14:17], v[14:15], off offset:512 nt
	s_nop 0
	global_load_dwordx4 v[18:21], v[18:19], off nt
	s_nop 0
	global_load_dwordx4 v[22:25], v[22:23], off nt
	s_nop 0
	global_load_dwordx4 v[26:29], v[26:27], off nt
	s_nop 0
	global_load_dwordx4 v[30:33], v[30:31], off nt
